# QKV GEMM K-loops: in a unit first K-iteration the two leading sub-phase waits use vmcnt(24) instead of vmcnt(8) so they do not wait for the previous unit 16 write-through epilogue stores (flag in an S
# baseline (speedup 1.0000x reference)
.LBB0_235:
	s_ashr_i32 s15, s14, 31
	s_lshl_b64 s[36:37], s[14:15], 18
	v_readlane_b32 s38, v254, 44
	v_readlane_b32 s39, v254, 45
	s_add_u32 s36, s38, s36
	s_addc_u32 s37, s39, s37
	s_and_b64 s[38:39], s[34:35], exec
	s_cselect_b32 s15, s37, s41
	s_cselect_b32 s54, s36, s40
	s_ashr_i32 s13, s12, 31
	s_lshl_b64 s[38:39], s[12:13], 18
	s_add_u32 s38, s16, s38
	s_addc_u32 s39, s17, s39
	s_and_b64 s[44:45], s[34:35], exec
	s_cselect_b32 s13, s39, s43
	s_cselect_b32 s55, s38, s42
	s_add_u32 s40, s40, 0x20080
	s_addc_u32 s41, s41, 0
	s_add_u32 s56, s42, 0x100
	v_mov_b32_e32 v64, 0
	s_addc_u32 s57, s43, 0
	s_mov_b32 s58, -2
	v_mov_b32_e32 v65, v64
	v_mov_b32_e32 v66, v64
	v_mov_b32_e32 v67, v64
	v_mov_b32_e32 v116, v64
	v_mov_b32_e32 v117, v64
	v_mov_b32_e32 v118, v64
	v_mov_b32_e32 v119, v64
	v_mov_b32_e32 v84, v64
	v_mov_b32_e32 v85, v64
	v_mov_b32_e32 v86, v64
	v_mov_b32_e32 v87, v64
	v_mov_b32_e32 v128, v64
	v_mov_b32_e32 v129, v64
	v_mov_b32_e32 v130, v64
	v_mov_b32_e32 v131, v64
	v_mov_b32_e32 v32, v64
	v_mov_b32_e32 v33, v64
	v_mov_b32_e32 v34, v64
	v_mov_b32_e32 v35, v64
	v_mov_b32_e32 v48, v64
	v_mov_b32_e32 v49, v64
	v_mov_b32_e32 v50, v64
	v_mov_b32_e32 v51, v64
	v_mov_b32_e32 v36, v64
	v_mov_b32_e32 v37, v64
	v_mov_b32_e32 v38, v64
	v_mov_b32_e32 v39, v64
	v_mov_b32_e32 v52, v64
	v_mov_b32_e32 v53, v64
	v_mov_b32_e32 v54, v64
	v_mov_b32_e32 v55, v64
	v_mov_b32_e32 v40, v64
	v_mov_b32_e32 v41, v64
	v_mov_b32_e32 v42, v64
	v_mov_b32_e32 v43, v64
	v_mov_b32_e32 v56, v64
	v_mov_b32_e32 v57, v64
	v_mov_b32_e32 v58, v64
	v_mov_b32_e32 v59, v64
	v_mov_b32_e32 v44, v64
	v_mov_b32_e32 v45, v64
	v_mov_b32_e32 v46, v64
	v_mov_b32_e32 v47, v64
	v_mov_b32_e32 v72, v64
	v_mov_b32_e32 v73, v64
	v_mov_b32_e32 v74, v64
	v_mov_b32_e32 v75, v64
	v_mov_b32_e32 v96, v64
	v_mov_b32_e32 v97, v64
	v_mov_b32_e32 v98, v64
	v_mov_b32_e32 v99, v64
	v_mov_b32_e32 v136, v64
	v_mov_b32_e32 v137, v64
	v_mov_b32_e32 v138, v64
	v_mov_b32_e32 v139, v64
	v_mov_b32_e32 v108, v64
	v_mov_b32_e32 v109, v64
	v_mov_b32_e32 v110, v64
	v_mov_b32_e32 v111, v64
	v_mov_b32_e32 v140, v64
	v_mov_b32_e32 v141, v64
	v_mov_b32_e32 v142, v64
	v_mov_b32_e32 v143, v64
	v_mov_b32_e32 v112, v64
	v_mov_b32_e32 v113, v64
	v_mov_b32_e32 v114, v64
	v_mov_b32_e32 v115, v64
	v_mov_b32_e32 v144, v64
	v_mov_b32_e32 v145, v64
	v_mov_b32_e32 v146, v64
	v_mov_b32_e32 v147, v64
	v_mov_b32_e32 v124, v64
	v_mov_b32_e32 v125, v64
	v_mov_b32_e32 v126, v64
	v_mov_b32_e32 v127, v64
	v_mov_b32_e32 v156, v64
	v_mov_b32_e32 v157, v64
	v_mov_b32_e32 v158, v64
	v_mov_b32_e32 v159, v64
	v_mov_b32_e32 v148, v64
	v_mov_b32_e32 v149, v64
	v_mov_b32_e32 v150, v64
	v_mov_b32_e32 v151, v64
	v_mov_b32_e32 v120, v64
	v_mov_b32_e32 v121, v64
	v_mov_b32_e32 v122, v64
	v_mov_b32_e32 v123, v64
	v_mov_b32_e32 v152, v64
	v_mov_b32_e32 v153, v64
	v_mov_b32_e32 v154, v64
	v_mov_b32_e32 v155, v64
	v_mov_b32_e32 v132, v64
	v_mov_b32_e32 v133, v64
	v_mov_b32_e32 v134, v64
	v_mov_b32_e32 v135, v64
	v_mov_b32_e32 v88, v64
	s_waitcnt lgkmcnt(0)
	v_mov_b32_e32 v89, v64
	v_mov_b32_e32 v90, v64
	v_mov_b32_e32 v91, v64
	v_mov_b32_e32 v60, v64
	v_mov_b32_e32 v61, v64
	v_mov_b32_e32 v62, v64
	v_mov_b32_e32 v63, v64
	v_mov_b32_e32 v92, v64
	v_mov_b32_e32 v93, v64
	v_mov_b32_e32 v94, v64
	v_mov_b32_e32 v95, v64
	v_mov_b32_e32 v68, v64
	v_mov_b32_e32 v69, v64
	v_mov_b32_e32 v70, v64
	v_mov_b32_e32 v71, v64
	v_mov_b32_e32 v100, v64
	v_mov_b32_e32 v101, v64
	v_mov_b32_e32 v102, v64
	v_mov_b32_e32 v103, v64
	v_mov_b32_e32 v76, v64
	v_mov_b32_e32 v77, v64
	v_mov_b32_e32 v78, v64
	v_mov_b32_e32 v79, v64
	v_mov_b32_e32 v104, v64
	v_mov_b32_e32 v105, v64
	v_mov_b32_e32 v106, v64
	v_mov_b32_e32 v107, v64
	v_mov_b32_e32 v80, v64
	v_mov_b32_e32 v81, v64
	v_mov_b32_e32 v82, v64
	v_mov_b32_e32 v83, v64
	s_mov_b32 s99, 1
.LBB0_236:
	ds_read_b128 v[20:23], v188
	ds_read_b128 v[24:27], v189
	ds_read_b128 v[16:19], v183
	ds_read_b128 v[0:3], v184
	ds_read_b128 v[28:31], v190
	ds_read_b128 v[4:7], v191
	ds_read_b128 v[8:11], v192
	ds_read_b128 v[12:15], v193
	s_add_u32 s42, s40, 0xfffe0080
	s_addc_u32 s43, s41, -1
	s_cmp_eq_u32 s58, 4
	s_cselect_b32 s45, s15, s43
	s_cselect_b32 s44, s54, s42
	s_cselect_b32 s43, s13, s57
	s_cselect_b32 s42, s55, s56
	v_lshl_add_u64 v[232:233], s[40:41], 0, v[168:169]
	s_add_i32 m0, s20, 0xc000
	ds_read_b128 v[174:177], v200
	ds_read_b128 v[178:181], v200 offset:1024
	ds_read_b128 v[208:211], v200 offset:2048
	ds_read_b128 v[212:215], v200 offset:3072
	ds_read_b128 v[216:219], v200 offset:4096
	ds_read_b128 v[220:223], v200 offset:5120
	ds_read_b128 v[224:227], v200 offset:6144
	ds_read_b128 v[228:231], v200 offset:7168
	global_load_lds_dwordx4 v[232:233], off
	v_lshl_add_u64 v[232:233], s[40:41], 0, v[170:171]
	s_add_i32 m0, s20, 0xe000
	s_nop 0
	global_load_lds_dwordx4 v[232:233], off
	s_waitcnt vmcnt(24)
	s_cmp_lg_u32 s99, 0
	s_cbranch_scc1 .Lfk0_a
	s_waitcnt vmcnt(8)
.Lfk0_a:
	s_waitcnt lgkmcnt(0)
	s_barrier
	s_setprio 1
	s_waitcnt lgkmcnt(0)
	v_mfma_f32_16x16x128_f8f6f4 v[156:159], v[16:23], v[174:181], v[156:159]
	v_mfma_f32_16x16x128_f8f6f4 v[124:127], v[24:31], v[174:181], v[124:127]
	v_mfma_f32_16x16x128_f8f6f4 v[144:147], v[16:23], v[208:215], v[144:147]
	v_mfma_f32_16x16x128_f8f6f4 v[112:115], v[24:31], v[208:215], v[112:115]
	v_mfma_f32_16x16x128_f8f6f4 v[140:143], v[16:23], v[216:223], v[140:143]
	v_mfma_f32_16x16x128_f8f6f4 v[108:111], v[24:31], v[216:223], v[108:111]
	v_mfma_f32_16x16x128_f8f6f4 v[136:139], v[16:23], v[224:231], v[136:139]
	v_mfma_f32_16x16x128_f8f6f4 v[96:99], v[24:31], v[224:231], v[96:99]
	s_setprio 0
	s_setprio 1
	v_mfma_f32_16x16x128_f8f6f4 v[72:75], v[0:7], v[174:181], v[72:75]
	v_mfma_f32_16x16x128_f8f6f4 v[44:47], v[8:15], v[174:181], v[44:47]
	v_mfma_f32_16x16x128_f8f6f4 v[56:59], v[0:7], v[208:215], v[56:59]
	v_mfma_f32_16x16x128_f8f6f4 v[40:43], v[8:15], v[208:215], v[40:43]
	v_mfma_f32_16x16x128_f8f6f4 v[52:55], v[0:7], v[216:223], v[52:55]
	v_mfma_f32_16x16x128_f8f6f4 v[36:39], v[8:15], v[216:223], v[36:39]
	v_mfma_f32_16x16x128_f8f6f4 v[48:51], v[0:7], v[224:231], v[48:51]
	v_mfma_f32_16x16x128_f8f6f4 v[32:35], v[8:15], v[224:231], v[32:35]
	s_setprio 0
	s_barrier
	s_mov_b32 m0, s21
	v_lshl_add_u64 v[174:175], s[42:43], 0, v[162:163]
	s_add_u32 s60, s42, 0x20000
	ds_read_b128 v[208:211], v200 offset:16384
	ds_read_b128 v[212:215], v200 offset:17408
	ds_read_b128 v[216:219], v200 offset:18432
	ds_read_b128 v[220:223], v200 offset:19456
	ds_read_b128 v[224:227], v200 offset:20480
	ds_read_b128 v[228:231], v200 offset:21504
	ds_read_b128 v[232:235], v200 offset:22528
	ds_read_b128 v[236:239], v200 offset:23552
	global_load_lds_dwordx4 v[174:175], off
	v_lshl_add_u64 v[176:177], s[42:43], 0, v[160:161]
	s_mov_b32 m0, s22
	s_addc_u32 s61, s43, 0
	global_load_lds_dwordx4 v[176:177], off
	v_lshl_add_u64 v[178:179], s[60:61], 0, v[162:163]
	s_mov_b32 m0, s23
	v_lshl_add_u64 v[180:181], s[44:45], 0, v[166:167]
	global_load_lds_dwordx4 v[178:179], off
	v_lshl_add_u64 v[178:179], s[60:61], 0, v[160:161]
	s_mov_b32 m0, s24
	s_nop 0
	global_load_lds_dwordx4 v[178:179], off
	v_lshl_add_u64 v[178:179], s[44:45], 0, v[164:165]
	s_mov_b32 m0, s20
	s_nop 0
	global_load_lds_dwordx4 v[178:179], off
	s_mov_b32 m0, s25
	s_nop 0
	global_load_lds_dwordx4 v[180:181], off
	s_waitcnt vmcnt(24)
	s_cmp_lg_u32 s99, 0
	s_cbranch_scc1 .Lfk0_b
	s_waitcnt vmcnt(8)
.Lfk0_b:
	s_mov_b32 s99, 0
	s_waitcnt lgkmcnt(0)
	s_barrier
	s_setprio 1
	s_waitcnt lgkmcnt(0)
	v_mfma_f32_16x16x128_f8f6f4 v[128:131], v[16:23], v[208:215], v[128:131]
	v_mfma_f32_16x16x128_f8f6f4 v[84:87], v[24:31], v[208:215], v[84:87]
	v_mfma_f32_16x16x128_f8f6f4 v[116:119], v[16:23], v[216:223], v[116:119]
	v_mfma_f32_16x16x128_f8f6f4 v[64:67], v[24:31], v[216:223], v[64:67]
	v_mfma_f32_16x16x128_f8f6f4 v[148:151], v[16:23], v[224:231], v[148:151]
	v_mfma_f32_16x16x128_f8f6f4 v[120:123], v[24:31], v[224:231], v[120:123]
	v_mfma_f32_16x16x128_f8f6f4 v[152:155], v[16:23], v[232:239], v[152:155]
	v_mfma_f32_16x16x128_f8f6f4 v[132:135], v[24:31], v[232:239], v[132:135]
	s_setprio 0
	s_setprio 1
	v_mfma_f32_16x16x128_f8f6f4 v[88:91], v[0:7], v[208:215], v[88:91]
	v_mfma_f32_16x16x128_f8f6f4 v[60:63], v[8:15], v[208:215], v[60:63]
	v_mfma_f32_16x16x128_f8f6f4 v[92:95], v[0:7], v[216:223], v[92:95]
	v_mfma_f32_16x16x128_f8f6f4 v[68:71], v[8:15], v[216:223], v[68:71]
	v_mfma_f32_16x16x128_f8f6f4 v[100:103], v[0:7], v[224:231], v[100:103]
	v_mfma_f32_16x16x128_f8f6f4 v[76:79], v[8:15], v[224:231], v[76:79]
	v_mfma_f32_16x16x128_f8f6f4 v[104:107], v[0:7], v[232:239], v[104:107]
	v_mfma_f32_16x16x128_f8f6f4 v[80:83], v[8:15], v[232:239], v[80:83]
	s_setprio 0
	s_barrier
	ds_read_b128 v[4:7], v194
	ds_read_b128 v[8:11], v195
	ds_read_b128 v[0:3], v185
	ds_read_b128 v[16:19], v186
	ds_read_b128 v[12:15], v196
	ds_read_b128 v[20:23], v197
	ds_read_b128 v[24:27], v198
	ds_read_b128 v[28:31], v199
	s_add_u32 s44, s44, 0x20000
	s_addc_u32 s45, s45, 0
	s_mov_b32 m0, s26
	v_lshl_add_u64 v[240:241], s[44:45], 0, v[164:165]
	ds_read_b128 v[208:211], v200 offset:32768
	ds_read_b128 v[212:215], v200 offset:33792
	ds_read_b128 v[216:219], v200 offset:34816
	ds_read_b128 v[220:223], v200 offset:35840
	ds_read_b128 v[224:227], v200 offset:36864
	ds_read_b128 v[228:231], v200 offset:37888
	ds_read_b128 v[232:235], v200 offset:38912
	ds_read_b128 v[236:239], v200 offset:39936
	global_load_lds_dwordx4 v[240:241], off
	v_lshl_add_u64 v[240:241], s[44:45], 0, v[166:167]
	s_mov_b32 m0, s27
	s_nop 0
	global_load_lds_dwordx4 v[240:241], off
	s_waitcnt vmcnt(8)
	s_waitcnt lgkmcnt(0)
	s_barrier
	s_setprio 1
	s_waitcnt lgkmcnt(0)
	v_mfma_f32_16x16x128_f8f6f4 v[156:159], v[0:7], v[208:215], v[156:159]
	v_mfma_f32_16x16x128_f8f6f4 v[124:127], v[8:15], v[208:215], v[124:127]
	v_mfma_f32_16x16x128_f8f6f4 v[144:147], v[0:7], v[216:223], v[144:147]
	v_mfma_f32_16x16x128_f8f6f4 v[112:115], v[8:15], v[216:223], v[112:115]
	v_mfma_f32_16x16x128_f8f6f4 v[140:143], v[0:7], v[224:231], v[140:143]
	v_mfma_f32_16x16x128_f8f6f4 v[108:111], v[8:15], v[224:231], v[108:111]
	v_mfma_f32_16x16x128_f8f6f4 v[136:139], v[0:7], v[232:239], v[136:139]
	v_mfma_f32_16x16x128_f8f6f4 v[96:99], v[8:15], v[232:239], v[96:99]
	s_setprio 0
	s_setprio 1
	v_mfma_f32_16x16x128_f8f6f4 v[72:75], v[16:23], v[208:215], v[72:75]
	v_mfma_f32_16x16x128_f8f6f4 v[44:47], v[24:31], v[208:215], v[44:47]
	v_mfma_f32_16x16x128_f8f6f4 v[56:59], v[16:23], v[216:223], v[56:59]
	v_mfma_f32_16x16x128_f8f6f4 v[40:43], v[24:31], v[216:223], v[40:43]
	v_mfma_f32_16x16x128_f8f6f4 v[52:55], v[16:23], v[224:231], v[52:55]
	v_mfma_f32_16x16x128_f8f6f4 v[36:39], v[24:31], v[224:231], v[36:39]
	v_mfma_f32_16x16x128_f8f6f4 v[48:51], v[16:23], v[232:239], v[48:51]
	v_mfma_f32_16x16x128_f8f6f4 v[32:35], v[24:31], v[232:239], v[32:35]
	s_setprio 0
	s_barrier
	s_mov_b32 m0, s29
	v_lshl_add_u64 v[174:175], v[174:175], 0, s[8:9]
	s_add_u32 s42, s42, 0x20080
	ds_read_b128 v[208:211], v200 offset:49152
	ds_read_b128 v[212:215], v200 offset:50176
	ds_read_b128 v[216:219], v200 offset:51200
	ds_read_b128 v[220:223], v200 offset:52224
	ds_read_b128 v[224:227], v200 offset:53248
	ds_read_b128 v[228:231], v200 offset:54272
	ds_read_b128 v[232:235], v200 offset:55296
	ds_read_b128 v[236:239], v200 offset:56320
	global_load_lds_dwordx4 v[174:175], off
	v_lshl_add_u64 v[174:175], v[176:177], 0, s[8:9]
	s_mov_b32 m0, s30
	s_addc_u32 s43, s43, 0
	global_load_lds_dwordx4 v[174:175], off
	v_lshl_add_u64 v[174:175], s[42:43], 0, v[162:163]
	s_mov_b32 m0, s46
	s_nop 0
	global_load_lds_dwordx4 v[174:175], off
	v_lshl_add_u64 v[174:175], s[42:43], 0, v[160:161]
	s_mov_b32 m0, s47
	s_nop 0
	global_load_lds_dwordx4 v[174:175], off
	v_lshl_add_u64 v[174:175], v[178:179], 0, s[8:9]
	s_mov_b32 m0, s31
	s_nop 0
	global_load_lds_dwordx4 v[174:175], off
	v_lshl_add_u64 v[174:175], v[180:181], 0, s[8:9]
	s_mov_b32 m0, s33
	s_nop 0
	global_load_lds_dwordx4 v[174:175], off
	s_waitcnt vmcnt(8)
	s_waitcnt lgkmcnt(0)
	s_barrier
	s_setprio 1
	s_waitcnt lgkmcnt(0)
	v_mfma_f32_16x16x128_f8f6f4 v[128:131], v[0:7], v[208:215], v[128:131]
	v_mfma_f32_16x16x128_f8f6f4 v[84:87], v[8:15], v[208:215], v[84:87]
	v_mfma_f32_16x16x128_f8f6f4 v[116:119], v[0:7], v[216:223], v[116:119]
	v_mfma_f32_16x16x128_f8f6f4 v[64:67], v[8:15], v[216:223], v[64:67]
	v_mfma_f32_16x16x128_f8f6f4 v[148:151], v[0:7], v[224:231], v[148:151]
	v_mfma_f32_16x16x128_f8f6f4 v[120:123], v[8:15], v[224:231], v[120:123]
	v_mfma_f32_16x16x128_f8f6f4 v[152:155], v[0:7], v[232:239], v[152:155]
	v_mfma_f32_16x16x128_f8f6f4 v[132:135], v[8:15], v[232:239], v[132:135]
	s_setprio 0
	s_setprio 1
	v_mfma_f32_16x16x128_f8f6f4 v[88:91], v[16:23], v[208:215], v[88:91]
	v_mfma_f32_16x16x128_f8f6f4 v[60:63], v[24:31], v[208:215], v[60:63]
	v_mfma_f32_16x16x128_f8f6f4 v[92:95], v[16:23], v[216:223], v[92:95]
	v_mfma_f32_16x16x128_f8f6f4 v[68:71], v[24:31], v[216:223], v[68:71]
	v_mfma_f32_16x16x128_f8f6f4 v[100:103], v[16:23], v[224:231], v[100:103]
	v_mfma_f32_16x16x128_f8f6f4 v[76:79], v[24:31], v[224:231], v[76:79]
	v_mfma_f32_16x16x128_f8f6f4 v[104:107], v[16:23], v[232:239], v[104:107]
	v_mfma_f32_16x16x128_f8f6f4 v[80:83], v[24:31], v[232:239], v[80:83]
	s_setprio 0
	s_barrier
	s_add_i32 s58, s58, 2
	s_add_u32 s40, s40, 0x100
	s_addc_u32 s41, s41, 0
	s_add_u32 s56, s56, 0x100
	s_addc_u32 s57, s57, 0
	s_cmp_gt_u32 s58, 5
	s_cbranch_scc0 .LBB0_236
	s_nop 15
	s_nop 7
	s_and_b64 vcc, exec, s[10:11]
	s_cbranch_vccz .LBB0_239
	s_barrier

.LBB0_1174:
	s_ashr_i32 s9, s8, 31
	s_lshl_b64 s[12:13], s[8:9], 18
	v_readlane_b32 s14, v254, 44
	v_readlane_b32 s15, v254, 45
	s_add_u32 s12, s14, s12
	s_addc_u32 s13, s15, s13
	s_and_b64 s[14:15], s[10:11], exec
	s_cselect_b32 s9, s13, s25
	s_cselect_b32 s46, s12, s24
	s_ashr_i32 s7, s6, 31
	s_lshl_b64 s[14:15], s[6:7], 18
	s_add_u32 s14, s18, s14
	s_addc_u32 s15, s19, s15
	s_and_b64 s[34:35], s[10:11], exec
	s_cselect_b32 s7, s15, s27
	s_cselect_b32 s47, s14, s26
	s_add_u32 s24, s24, 0x20080
	s_addc_u32 s25, s25, 0
	s_add_u32 s48, s26, 0x100
	v_mov_b32_e32 v48, 0
	s_addc_u32 s49, s27, 0
	s_mov_b32 s50, -2
	v_mov_b32_e32 v49, v48
	v_mov_b32_e32 v50, v48
	v_mov_b32_e32 v51, v48
	v_mov_b32_e32 v52, v48
	v_mov_b32_e32 v53, v48
	v_mov_b32_e32 v54, v48
	v_mov_b32_e32 v55, v48
	v_mov_b32_e32 v72, v48
	v_mov_b32_e32 v73, v48
	v_mov_b32_e32 v74, v48
	v_mov_b32_e32 v75, v48
	v_mov_b32_e32 v76, v48
	v_mov_b32_e32 v77, v48
	v_mov_b32_e32 v78, v48
	v_mov_b32_e32 v79, v48
	v_mov_b32_e32 v88, v48
	v_mov_b32_e32 v89, v48
	v_mov_b32_e32 v90, v48
	v_mov_b32_e32 v91, v48
	v_mov_b32_e32 v92, v48
	v_mov_b32_e32 v93, v48
	v_mov_b32_e32 v94, v48
	v_mov_b32_e32 v95, v48
	v_mov_b32_e32 v108, v48
	v_mov_b32_e32 v109, v48
	v_mov_b32_e32 v110, v48
	v_mov_b32_e32 v111, v48
	v_mov_b32_e32 v116, v48
	v_mov_b32_e32 v117, v48
	v_mov_b32_e32 v118, v48
	v_mov_b32_e32 v119, v48
	v_mov_b32_e32 v124, v48
	v_mov_b32_e32 v125, v48
	v_mov_b32_e32 v126, v48
	v_mov_b32_e32 v127, v48
	v_mov_b32_e32 v132, v48
	v_mov_b32_e32 v133, v48
	v_mov_b32_e32 v134, v48
	v_mov_b32_e32 v135, v48
	v_mov_b32_e32 v140, v48
	v_mov_b32_e32 v141, v48
	v_mov_b32_e32 v142, v48
	v_mov_b32_e32 v143, v48
	v_mov_b32_e32 v148, v48
	v_mov_b32_e32 v149, v48
	v_mov_b32_e32 v150, v48
	v_mov_b32_e32 v151, v48
	v_mov_b32_e32 v104, v48
	v_mov_b32_e32 v105, v48
	v_mov_b32_e32 v106, v48
	v_mov_b32_e32 v107, v48
	v_mov_b32_e32 v112, v48
	v_mov_b32_e32 v113, v48
	v_mov_b32_e32 v114, v48
	v_mov_b32_e32 v115, v48
	v_mov_b32_e32 v120, v48
	v_mov_b32_e32 v121, v48
	v_mov_b32_e32 v122, v48
	v_mov_b32_e32 v123, v48
	v_mov_b32_e32 v128, v48
	v_mov_b32_e32 v129, v48
	v_mov_b32_e32 v130, v48
	v_mov_b32_e32 v131, v48
	v_mov_b32_e32 v136, v48
	v_mov_b32_e32 v137, v48
	v_mov_b32_e32 v138, v48
	v_mov_b32_e32 v139, v48
	v_mov_b32_e32 v144, v48
	v_mov_b32_e32 v145, v48
	v_mov_b32_e32 v146, v48
	v_mov_b32_e32 v147, v48
	v_mov_b32_e32 v152, v48
	v_mov_b32_e32 v153, v48
	v_mov_b32_e32 v154, v48
	v_mov_b32_e32 v155, v48
	v_mov_b32_e32 v156, v48
	v_mov_b32_e32 v157, v48
	v_mov_b32_e32 v158, v48
	v_mov_b32_e32 v159, v48
	v_mov_b32_e32 v60, v48
	v_mov_b32_e32 v61, v48
	v_mov_b32_e32 v62, v48
	v_mov_b32_e32 v63, v48
	v_mov_b32_e32 v56, v48
	v_mov_b32_e32 v57, v48
	v_mov_b32_e32 v58, v48
	v_mov_b32_e32 v59, v48
	v_mov_b32_e32 v36, v48
	v_mov_b32_e32 v37, v48
	v_mov_b32_e32 v38, v48
	v_mov_b32_e32 v39, v48
	v_mov_b32_e32 v32, v48
	v_mov_b32_e32 v33, v48
	v_mov_b32_e32 v34, v48
	v_mov_b32_e32 v35, v48
	v_mov_b32_e32 v100, v48
	v_mov_b32_e32 v101, v48
	v_mov_b32_e32 v102, v48
	v_mov_b32_e32 v103, v48
	v_mov_b32_e32 v96, v48
	v_mov_b32_e32 v97, v48
	v_mov_b32_e32 v98, v48
	v_mov_b32_e32 v99, v48
	v_mov_b32_e32 v84, v48
	v_mov_b32_e32 v85, v48
	v_mov_b32_e32 v86, v48
	v_mov_b32_e32 v87, v48
	v_mov_b32_e32 v80, v48
	v_mov_b32_e32 v81, v48
	v_mov_b32_e32 v82, v48
	v_mov_b32_e32 v83, v48
	v_mov_b32_e32 v68, v48
	v_mov_b32_e32 v69, v48
	v_mov_b32_e32 v70, v48
	v_mov_b32_e32 v71, v48
	v_mov_b32_e32 v64, v48
	v_mov_b32_e32 v65, v48
	v_mov_b32_e32 v66, v48
	v_mov_b32_e32 v67, v48
	v_mov_b32_e32 v44, v48
	v_mov_b32_e32 v45, v48
	v_mov_b32_e32 v46, v48
	v_mov_b32_e32 v47, v48
	v_mov_b32_e32 v40, v48
	v_mov_b32_e32 v41, v48
	v_mov_b32_e32 v42, v48
	v_mov_b32_e32 v43, v48
	s_mov_b32 s95, 1
.LBB0_1175:
	ds_read_b128 v[20:23], v188
	ds_read_b128 v[24:27], v189
	ds_read_b128 v[16:19], v183
	ds_read_b128 v[0:3], v184
	ds_read_b128 v[28:31], v190
	ds_read_b128 v[4:7], v191
	ds_read_b128 v[8:11], v192
	ds_read_b128 v[12:15], v193
	s_add_u32 s26, s24, 0xfffe0080
	s_addc_u32 s27, s25, -1
	s_cmp_eq_u32 s50, 4
	s_cselect_b32 s35, s9, s27
	s_cselect_b32 s34, s46, s26
	s_cselect_b32 s27, s7, s49
	s_cselect_b32 s26, s47, s48
	v_lshl_add_u64 v[228:229], s[24:25], 0, v[168:169]
	s_add_i32 m0, s17, 0xc000
	ds_read_b128 v[174:177], v200
	ds_read_b128 v[178:181], v200 offset:1024
	ds_read_b128 v[204:207], v200 offset:2048
	ds_read_b128 v[208:211], v200 offset:3072
	ds_read_b128 v[212:215], v200 offset:4096
	ds_read_b128 v[216:219], v200 offset:5120
	ds_read_b128 v[220:223], v200 offset:6144
	ds_read_b128 v[224:227], v200 offset:7168
	global_load_lds_dwordx4 v[228:229], off
	v_lshl_add_u64 v[228:229], s[24:25], 0, v[170:171]
	s_add_i32 m0, s17, 0xe000
	s_nop 0
	global_load_lds_dwordx4 v[228:229], off
	s_waitcnt vmcnt(24)
	s_cmp_lg_u32 s95, 0
	s_cbranch_scc1 .Lfk1_a
	s_waitcnt vmcnt(8)
.Lfk1_a:
	s_waitcnt lgkmcnt(0)
	s_barrier
	s_setprio 1
	s_waitcnt lgkmcnt(0)
	v_mfma_f32_16x16x128_f8f6f4 v[156:159], v[16:23], v[174:181], v[156:159]
	v_mfma_f32_16x16x128_f8f6f4 v[152:155], v[24:31], v[174:181], v[152:155]
	v_mfma_f32_16x16x128_f8f6f4 v[144:147], v[16:23], v[204:211], v[144:147]
	v_mfma_f32_16x16x128_f8f6f4 v[136:139], v[24:31], v[204:211], v[136:139]
	v_mfma_f32_16x16x128_f8f6f4 v[128:131], v[16:23], v[212:219], v[128:131]
	v_mfma_f32_16x16x128_f8f6f4 v[120:123], v[24:31], v[212:219], v[120:123]
	v_mfma_f32_16x16x128_f8f6f4 v[112:115], v[16:23], v[220:227], v[112:115]
	v_mfma_f32_16x16x128_f8f6f4 v[104:107], v[24:31], v[220:227], v[104:107]
	s_setprio 0
	s_setprio 1
	v_mfma_f32_16x16x128_f8f6f4 v[148:151], v[0:7], v[174:181], v[148:151]
	v_mfma_f32_16x16x128_f8f6f4 v[140:143], v[8:15], v[174:181], v[140:143]
	v_mfma_f32_16x16x128_f8f6f4 v[132:135], v[0:7], v[204:211], v[132:135]
	v_mfma_f32_16x16x128_f8f6f4 v[124:127], v[8:15], v[204:211], v[124:127]
	v_mfma_f32_16x16x128_f8f6f4 v[116:119], v[0:7], v[212:219], v[116:119]
	v_mfma_f32_16x16x128_f8f6f4 v[108:111], v[8:15], v[212:219], v[108:111]
	v_mfma_f32_16x16x128_f8f6f4 v[92:95], v[0:7], v[220:227], v[92:95]
	v_mfma_f32_16x16x128_f8f6f4 v[88:91], v[8:15], v[220:227], v[88:91]
	s_setprio 0
	s_barrier
	s_mov_b32 m0, s22
	v_lshl_add_u64 v[174:175], s[26:27], 0, v[162:163]
	s_add_u32 s52, s26, 0x20000
	ds_read_b128 v[204:207], v200 offset:16384
	ds_read_b128 v[208:211], v200 offset:17408
	ds_read_b128 v[212:215], v200 offset:18432
	ds_read_b128 v[216:219], v200 offset:19456
	ds_read_b128 v[220:223], v200 offset:20480
	ds_read_b128 v[224:227], v200 offset:21504
	ds_read_b128 v[228:231], v200 offset:22528
	ds_read_b128 v[232:235], v200 offset:23552
	global_load_lds_dwordx4 v[174:175], off
	v_lshl_add_u64 v[176:177], s[26:27], 0, v[160:161]
	s_mov_b32 m0, s23
	s_addc_u32 s53, s27, 0
	global_load_lds_dwordx4 v[176:177], off
	v_lshl_add_u64 v[178:179], s[52:53], 0, v[162:163]
	s_mov_b32 m0, s28
	v_lshl_add_u64 v[180:181], s[34:35], 0, v[166:167]
	global_load_lds_dwordx4 v[178:179], off
	v_lshl_add_u64 v[178:179], s[52:53], 0, v[160:161]
	s_mov_b32 m0, s29
	s_nop 0
	global_load_lds_dwordx4 v[178:179], off
	v_lshl_add_u64 v[178:179], s[34:35], 0, v[164:165]
	s_mov_b32 m0, s17
	s_nop 0
	global_load_lds_dwordx4 v[178:179], off
	s_mov_b32 m0, s30
	s_nop 0
	global_load_lds_dwordx4 v[180:181], off
	s_waitcnt vmcnt(24)
	s_cmp_lg_u32 s95, 0
	s_cbranch_scc1 .Lfk1_b
	s_waitcnt vmcnt(8)
.Lfk1_b:
	s_mov_b32 s95, 0
	s_waitcnt lgkmcnt(0)
	s_barrier
	s_setprio 1
	s_waitcnt lgkmcnt(0)
	v_mfma_f32_16x16x128_f8f6f4 v[76:79], v[16:23], v[204:211], v[76:79]
	v_mfma_f32_16x16x128_f8f6f4 v[72:75], v[24:31], v[204:211], v[72:75]
	v_mfma_f32_16x16x128_f8f6f4 v[52:55], v[16:23], v[212:219], v[52:55]
	v_mfma_f32_16x16x128_f8f6f4 v[48:51], v[24:31], v[212:219], v[48:51]
	v_mfma_f32_16x16x128_f8f6f4 v[60:63], v[16:23], v[220:227], v[60:63]
	v_mfma_f32_16x16x128_f8f6f4 v[56:59], v[24:31], v[220:227], v[56:59]
	v_mfma_f32_16x16x128_f8f6f4 v[36:39], v[16:23], v[228:235], v[36:39]
	v_mfma_f32_16x16x128_f8f6f4 v[32:35], v[24:31], v[228:235], v[32:35]
	s_setprio 0
	s_setprio 1
	v_mfma_f32_16x16x128_f8f6f4 v[100:103], v[0:7], v[204:211], v[100:103]
	v_mfma_f32_16x16x128_f8f6f4 v[96:99], v[8:15], v[204:211], v[96:99]
	v_mfma_f32_16x16x128_f8f6f4 v[84:87], v[0:7], v[212:219], v[84:87]
	v_mfma_f32_16x16x128_f8f6f4 v[80:83], v[8:15], v[212:219], v[80:83]
	v_mfma_f32_16x16x128_f8f6f4 v[68:71], v[0:7], v[220:227], v[68:71]
	v_mfma_f32_16x16x128_f8f6f4 v[64:67], v[8:15], v[220:227], v[64:67]
	v_mfma_f32_16x16x128_f8f6f4 v[44:47], v[0:7], v[228:235], v[44:47]
	v_mfma_f32_16x16x128_f8f6f4 v[40:43], v[8:15], v[228:235], v[40:43]
	s_setprio 0
	s_barrier
	ds_read_b128 v[4:7], v194
	ds_read_b128 v[8:11], v195
	ds_read_b128 v[0:3], v185
	ds_read_b128 v[16:19], v186
	ds_read_b128 v[12:15], v196
	ds_read_b128 v[20:23], v197
	ds_read_b128 v[24:27], v198
	ds_read_b128 v[28:31], v199
	s_add_u32 s34, s34, 0x20000
	s_addc_u32 s35, s35, 0
	s_mov_b32 m0, s31
	v_lshl_add_u64 v[236:237], s[34:35], 0, v[164:165]
	ds_read_b128 v[204:207], v200 offset:32768
	ds_read_b128 v[208:211], v200 offset:33792
	ds_read_b128 v[212:215], v200 offset:34816
	ds_read_b128 v[216:219], v200 offset:35840
	ds_read_b128 v[220:223], v200 offset:36864
	ds_read_b128 v[224:227], v200 offset:37888
	ds_read_b128 v[228:231], v200 offset:38912
	ds_read_b128 v[232:235], v200 offset:39936
	global_load_lds_dwordx4 v[236:237], off
	v_lshl_add_u64 v[236:237], s[34:35], 0, v[166:167]
	s_mov_b32 m0, s33
	s_nop 0
	global_load_lds_dwordx4 v[236:237], off
	s_waitcnt vmcnt(8)
	s_waitcnt lgkmcnt(0)
	s_barrier
	s_setprio 1
	s_waitcnt lgkmcnt(0)
	v_mfma_f32_16x16x128_f8f6f4 v[156:159], v[0:7], v[204:211], v[156:159]
	v_mfma_f32_16x16x128_f8f6f4 v[152:155], v[8:15], v[204:211], v[152:155]
	v_mfma_f32_16x16x128_f8f6f4 v[144:147], v[0:7], v[212:219], v[144:147]
	v_mfma_f32_16x16x128_f8f6f4 v[136:139], v[8:15], v[212:219], v[136:139]
	v_mfma_f32_16x16x128_f8f6f4 v[128:131], v[0:7], v[220:227], v[128:131]
	v_mfma_f32_16x16x128_f8f6f4 v[120:123], v[8:15], v[220:227], v[120:123]
	v_mfma_f32_16x16x128_f8f6f4 v[112:115], v[0:7], v[228:235], v[112:115]
	v_mfma_f32_16x16x128_f8f6f4 v[104:107], v[8:15], v[228:235], v[104:107]
	s_setprio 0
	s_setprio 1
	v_mfma_f32_16x16x128_f8f6f4 v[148:151], v[16:23], v[204:211], v[148:151]
	v_mfma_f32_16x16x128_f8f6f4 v[140:143], v[24:31], v[204:211], v[140:143]
	v_mfma_f32_16x16x128_f8f6f4 v[132:135], v[16:23], v[212:219], v[132:135]
	v_mfma_f32_16x16x128_f8f6f4 v[124:127], v[24:31], v[212:219], v[124:127]
	v_mfma_f32_16x16x128_f8f6f4 v[116:119], v[16:23], v[220:227], v[116:119]
	v_mfma_f32_16x16x128_f8f6f4 v[108:111], v[24:31], v[220:227], v[108:111]
	v_mfma_f32_16x16x128_f8f6f4 v[92:95], v[16:23], v[228:235], v[92:95]
	v_mfma_f32_16x16x128_f8f6f4 v[88:91], v[24:31], v[228:235], v[88:91]
	s_setprio 0
	s_barrier
	s_mov_b32 m0, s37
	v_lshl_add_u64 v[174:175], v[174:175], 0, s[2:3]
	s_add_u32 s26, s26, 0x20080
	ds_read_b128 v[204:207], v200 offset:49152
	ds_read_b128 v[208:211], v200 offset:50176
	ds_read_b128 v[212:215], v200 offset:51200
	ds_read_b128 v[216:219], v200 offset:52224
	ds_read_b128 v[220:223], v200 offset:53248
	ds_read_b128 v[224:227], v200 offset:54272
	ds_read_b128 v[228:231], v200 offset:55296
	ds_read_b128 v[232:235], v200 offset:56320
	global_load_lds_dwordx4 v[174:175], off
	v_lshl_add_u64 v[174:175], v[176:177], 0, s[2:3]
	s_mov_b32 m0, s38
	s_addc_u32 s27, s27, 0
	global_load_lds_dwordx4 v[174:175], off
	v_lshl_add_u64 v[174:175], s[26:27], 0, v[162:163]
	s_mov_b32 m0, s41
	s_nop 0
	global_load_lds_dwordx4 v[174:175], off
	v_lshl_add_u64 v[174:175], s[26:27], 0, v[160:161]
	s_mov_b32 m0, s42
	s_nop 0
	global_load_lds_dwordx4 v[174:175], off
	v_lshl_add_u64 v[174:175], v[178:179], 0, s[2:3]
	s_mov_b32 m0, s39
	s_nop 0
	global_load_lds_dwordx4 v[174:175], off
	v_lshl_add_u64 v[174:175], v[180:181], 0, s[2:3]
	s_mov_b32 m0, s40
	s_nop 0
	global_load_lds_dwordx4 v[174:175], off
	s_waitcnt vmcnt(8)
	s_waitcnt lgkmcnt(0)
	s_barrier
	s_setprio 1
	s_waitcnt lgkmcnt(0)
	v_mfma_f32_16x16x128_f8f6f4 v[76:79], v[0:7], v[204:211], v[76:79]
	v_mfma_f32_16x16x128_f8f6f4 v[72:75], v[8:15], v[204:211], v[72:75]
	v_mfma_f32_16x16x128_f8f6f4 v[52:55], v[0:7], v[212:219], v[52:55]
	v_mfma_f32_16x16x128_f8f6f4 v[48:51], v[8:15], v[212:219], v[48:51]
	v_mfma_f32_16x16x128_f8f6f4 v[60:63], v[0:7], v[220:227], v[60:63]
	v_mfma_f32_16x16x128_f8f6f4 v[56:59], v[8:15], v[220:227], v[56:59]
	v_mfma_f32_16x16x128_f8f6f4 v[36:39], v[0:7], v[228:235], v[36:39]
	v_mfma_f32_16x16x128_f8f6f4 v[32:35], v[8:15], v[228:235], v[32:35]
	s_setprio 0
	s_setprio 1
	v_mfma_f32_16x16x128_f8f6f4 v[100:103], v[16:23], v[204:211], v[100:103]
	v_mfma_f32_16x16x128_f8f6f4 v[96:99], v[24:31], v[204:211], v[96:99]
	v_mfma_f32_16x16x128_f8f6f4 v[84:87], v[16:23], v[212:219], v[84:87]
	v_mfma_f32_16x16x128_f8f6f4 v[80:83], v[24:31], v[212:219], v[80:83]
	v_mfma_f32_16x16x128_f8f6f4 v[68:71], v[16:23], v[220:227], v[68:71]
	v_mfma_f32_16x16x128_f8f6f4 v[64:67], v[24:31], v[220:227], v[64:67]
	v_mfma_f32_16x16x128_f8f6f4 v[44:47], v[16:23], v[228:235], v[44:47]
	v_mfma_f32_16x16x128_f8f6f4 v[40:43], v[24:31], v[228:235], v[40:43]
	s_setprio 0
	s_barrier
	s_add_i32 s50, s50, 2
	s_add_u32 s24, s24, 0x100
	s_addc_u32 s25, s25, 0
	s_add_u32 s48, s48, 0x100
	s_addc_u32 s49, s49, 0
	s_cmp_gt_u32 s50, 5
	s_cbranch_scc0 .LBB0_1175
	s_nop 15
	s_nop 7
	s_and_b64 vcc, exec, s[4:5]
	s_cbranch_vccz .LBB0_1178
	s_barrier

.LBB0_2051:
	s_ashr_i32 s9, s8, 31
	s_lshl_b64 s[12:13], s[8:9], 18
	v_readlane_b32 s14, v254, 44
	v_readlane_b32 s15, v254, 45
	s_add_u32 s12, s14, s12
	s_addc_u32 s13, s15, s13
	s_and_b64 s[14:15], s[10:11], exec
	s_cselect_b32 s9, s13, s25
	s_cselect_b32 s46, s12, s24
	s_ashr_i32 s7, s6, 31
	s_lshl_b64 s[14:15], s[6:7], 18
	s_add_u32 s14, s18, s14
	s_addc_u32 s15, s19, s15
	s_and_b64 s[28:29], s[10:11], exec
	s_cselect_b32 s7, s15, s27
	s_cselect_b32 s47, s14, s26
	s_add_u32 s24, s24, 0x20080
	s_addc_u32 s25, s25, 0
	s_add_u32 s48, s26, 0x100
	v_mov_b32_e32 v48, 0
	s_addc_u32 s49, s27, 0
	s_mov_b32 s50, -2
	v_mov_b32_e32 v49, v48
	v_mov_b32_e32 v50, v48
	v_mov_b32_e32 v51, v48
	v_mov_b32_e32 v52, v48
	v_mov_b32_e32 v53, v48
	v_mov_b32_e32 v54, v48
	v_mov_b32_e32 v55, v48
	v_mov_b32_e32 v72, v48
	v_mov_b32_e32 v73, v48
	v_mov_b32_e32 v74, v48
	v_mov_b32_e32 v75, v48
	v_mov_b32_e32 v76, v48
	v_mov_b32_e32 v77, v48
	v_mov_b32_e32 v78, v48
	v_mov_b32_e32 v79, v48
	v_mov_b32_e32 v88, v48
	v_mov_b32_e32 v89, v48
	v_mov_b32_e32 v90, v48
	v_mov_b32_e32 v91, v48
	v_mov_b32_e32 v92, v48
	v_mov_b32_e32 v93, v48
	v_mov_b32_e32 v94, v48
	v_mov_b32_e32 v95, v48
	v_mov_b32_e32 v108, v48
	v_mov_b32_e32 v109, v48
	v_mov_b32_e32 v110, v48
	v_mov_b32_e32 v111, v48
	v_mov_b32_e32 v116, v48
	v_mov_b32_e32 v117, v48
	v_mov_b32_e32 v118, v48
	v_mov_b32_e32 v119, v48
	v_mov_b32_e32 v124, v48
	v_mov_b32_e32 v125, v48
	v_mov_b32_e32 v126, v48
	v_mov_b32_e32 v127, v48
	v_mov_b32_e32 v132, v48
	v_mov_b32_e32 v133, v48
	v_mov_b32_e32 v134, v48
	v_mov_b32_e32 v135, v48
	v_mov_b32_e32 v140, v48
	v_mov_b32_e32 v141, v48
	v_mov_b32_e32 v142, v48
	v_mov_b32_e32 v143, v48
	v_mov_b32_e32 v148, v48
	v_mov_b32_e32 v149, v48
	v_mov_b32_e32 v150, v48
	v_mov_b32_e32 v151, v48
	v_mov_b32_e32 v104, v48
	v_mov_b32_e32 v105, v48
	v_mov_b32_e32 v106, v48
	v_mov_b32_e32 v107, v48
	v_mov_b32_e32 v112, v48
	v_mov_b32_e32 v113, v48
	v_mov_b32_e32 v114, v48
	v_mov_b32_e32 v115, v48
	v_mov_b32_e32 v120, v48
	v_mov_b32_e32 v121, v48
	v_mov_b32_e32 v122, v48
	v_mov_b32_e32 v123, v48
	v_mov_b32_e32 v128, v48
	v_mov_b32_e32 v129, v48
	v_mov_b32_e32 v130, v48
	v_mov_b32_e32 v131, v48
	v_mov_b32_e32 v136, v48
	v_mov_b32_e32 v137, v48
	v_mov_b32_e32 v138, v48
	v_mov_b32_e32 v139, v48
	v_mov_b32_e32 v144, v48
	v_mov_b32_e32 v145, v48
	v_mov_b32_e32 v146, v48
	v_mov_b32_e32 v147, v48
	v_mov_b32_e32 v152, v48
	v_mov_b32_e32 v153, v48
	v_mov_b32_e32 v154, v48
	v_mov_b32_e32 v155, v48
	v_mov_b32_e32 v156, v48
	v_mov_b32_e32 v157, v48
	v_mov_b32_e32 v158, v48
	v_mov_b32_e32 v159, v48
	v_mov_b32_e32 v60, v48
	v_mov_b32_e32 v61, v48
	v_mov_b32_e32 v62, v48
	v_mov_b32_e32 v63, v48
	v_mov_b32_e32 v56, v48
	v_mov_b32_e32 v57, v48
	v_mov_b32_e32 v58, v48
	v_mov_b32_e32 v59, v48
	v_mov_b32_e32 v36, v48
	v_mov_b32_e32 v37, v48
	v_mov_b32_e32 v38, v48
	v_mov_b32_e32 v39, v48
	v_mov_b32_e32 v32, v48
	v_mov_b32_e32 v33, v48
	v_mov_b32_e32 v34, v48
	v_mov_b32_e32 v35, v48
	v_mov_b32_e32 v100, v48
	v_mov_b32_e32 v101, v48
	v_mov_b32_e32 v102, v48
	v_mov_b32_e32 v103, v48
	v_mov_b32_e32 v96, v48
	v_mov_b32_e32 v97, v48
	v_mov_b32_e32 v98, v48
	v_mov_b32_e32 v99, v48
	v_mov_b32_e32 v84, v48
	v_mov_b32_e32 v85, v48
	v_mov_b32_e32 v86, v48
	v_mov_b32_e32 v87, v48
	v_mov_b32_e32 v80, v48
	v_mov_b32_e32 v81, v48
	v_mov_b32_e32 v82, v48
	v_mov_b32_e32 v83, v48
	v_mov_b32_e32 v68, v48
	v_mov_b32_e32 v69, v48
	v_mov_b32_e32 v70, v48
	v_mov_b32_e32 v71, v48
	v_mov_b32_e32 v64, v48
	v_mov_b32_e32 v65, v48
	v_mov_b32_e32 v66, v48
	v_mov_b32_e32 v67, v48
	v_mov_b32_e32 v44, v48
	v_mov_b32_e32 v45, v48
	v_mov_b32_e32 v46, v48
	v_mov_b32_e32 v47, v48
	v_mov_b32_e32 v40, v48
	v_mov_b32_e32 v41, v48
	v_mov_b32_e32 v42, v48
	v_mov_b32_e32 v43, v48
	s_mov_b32 s95, 1
.LBB0_2052:
	ds_read_b128 v[20:23], v188
	ds_read_b128 v[24:27], v189
	ds_read_b128 v[16:19], v183
	ds_read_b128 v[0:3], v184
	ds_read_b128 v[28:31], v190
	ds_read_b128 v[4:7], v191
	ds_read_b128 v[8:11], v192
	ds_read_b128 v[12:15], v193
	s_add_u32 s26, s24, 0xfffe0080
	s_addc_u32 s27, s25, -1
	s_cmp_eq_u32 s50, 4
	s_cselect_b32 s29, s9, s27
	s_cselect_b32 s28, s46, s26
	s_cselect_b32 s27, s7, s49
	s_cselect_b32 s26, s47, s48
	v_lshl_add_u64 v[228:229], s[24:25], 0, v[168:169]
	s_add_i32 m0, s17, 0xc000
	ds_read_b128 v[174:177], v200
	ds_read_b128 v[178:181], v200 offset:1024
	ds_read_b128 v[204:207], v200 offset:2048
	ds_read_b128 v[208:211], v200 offset:3072
	ds_read_b128 v[212:215], v200 offset:4096
	ds_read_b128 v[216:219], v200 offset:5120
	ds_read_b128 v[220:223], v200 offset:6144
	ds_read_b128 v[224:227], v200 offset:7168
	global_load_lds_dwordx4 v[228:229], off
	v_lshl_add_u64 v[228:229], s[24:25], 0, v[170:171]
	s_add_i32 m0, s17, 0xe000
	s_nop 0
	global_load_lds_dwordx4 v[228:229], off
	s_waitcnt vmcnt(24)
	s_cmp_lg_u32 s95, 0
	s_cbranch_scc1 .Lfk2_a
	s_waitcnt vmcnt(8)
.Lfk2_a:
	s_waitcnt lgkmcnt(0)
	s_barrier
	s_setprio 1
	s_waitcnt lgkmcnt(0)
	v_mfma_f32_16x16x128_f8f6f4 v[156:159], v[16:23], v[174:181], v[156:159]
	v_mfma_f32_16x16x128_f8f6f4 v[152:155], v[24:31], v[174:181], v[152:155]
	v_mfma_f32_16x16x128_f8f6f4 v[144:147], v[16:23], v[204:211], v[144:147]
	v_mfma_f32_16x16x128_f8f6f4 v[136:139], v[24:31], v[204:211], v[136:139]
	v_mfma_f32_16x16x128_f8f6f4 v[128:131], v[16:23], v[212:219], v[128:131]
	v_mfma_f32_16x16x128_f8f6f4 v[120:123], v[24:31], v[212:219], v[120:123]
	v_mfma_f32_16x16x128_f8f6f4 v[112:115], v[16:23], v[220:227], v[112:115]
	v_mfma_f32_16x16x128_f8f6f4 v[104:107], v[24:31], v[220:227], v[104:107]
	s_setprio 0
	s_setprio 1
	v_mfma_f32_16x16x128_f8f6f4 v[148:151], v[0:7], v[174:181], v[148:151]
	v_mfma_f32_16x16x128_f8f6f4 v[140:143], v[8:15], v[174:181], v[140:143]
	v_mfma_f32_16x16x128_f8f6f4 v[132:135], v[0:7], v[204:211], v[132:135]
	v_mfma_f32_16x16x128_f8f6f4 v[124:127], v[8:15], v[204:211], v[124:127]
	v_mfma_f32_16x16x128_f8f6f4 v[116:119], v[0:7], v[212:219], v[116:119]
	v_mfma_f32_16x16x128_f8f6f4 v[108:111], v[8:15], v[212:219], v[108:111]
	v_mfma_f32_16x16x128_f8f6f4 v[92:95], v[0:7], v[220:227], v[92:95]
	v_mfma_f32_16x16x128_f8f6f4 v[88:91], v[8:15], v[220:227], v[88:91]
	s_setprio 0
	s_barrier
	s_mov_b32 m0, s22
	v_lshl_add_u64 v[174:175], s[26:27], 0, v[162:163]
	s_add_u32 s52, s26, 0x20000
	ds_read_b128 v[204:207], v200 offset:16384
	ds_read_b128 v[208:211], v200 offset:17408
	ds_read_b128 v[212:215], v200 offset:18432
	ds_read_b128 v[216:219], v200 offset:19456
	ds_read_b128 v[220:223], v200 offset:20480
	ds_read_b128 v[224:227], v200 offset:21504
	ds_read_b128 v[228:231], v200 offset:22528
	ds_read_b128 v[232:235], v200 offset:23552
	global_load_lds_dwordx4 v[174:175], off
	v_lshl_add_u64 v[176:177], s[26:27], 0, v[160:161]
	s_mov_b32 m0, s23
	s_addc_u32 s53, s27, 0
	global_load_lds_dwordx4 v[176:177], off
	v_lshl_add_u64 v[178:179], s[52:53], 0, v[162:163]
	s_mov_b32 m0, s30
	v_lshl_add_u64 v[180:181], s[28:29], 0, v[166:167]
	global_load_lds_dwordx4 v[178:179], off
	v_lshl_add_u64 v[178:179], s[52:53], 0, v[160:161]
	s_mov_b32 m0, s31
	s_nop 0
	global_load_lds_dwordx4 v[178:179], off
	v_lshl_add_u64 v[178:179], s[28:29], 0, v[164:165]
	s_mov_b32 m0, s17
	s_nop 0
	global_load_lds_dwordx4 v[178:179], off
	s_mov_b32 m0, s33
	s_nop 0
	global_load_lds_dwordx4 v[180:181], off
	s_waitcnt vmcnt(24)
	s_cmp_lg_u32 s95, 0
	s_cbranch_scc1 .Lfk2_b
	s_waitcnt vmcnt(8)
.Lfk2_b:
	s_mov_b32 s95, 0
	s_waitcnt lgkmcnt(0)
	s_barrier
	s_setprio 1
	s_waitcnt lgkmcnt(0)
	v_mfma_f32_16x16x128_f8f6f4 v[76:79], v[16:23], v[204:211], v[76:79]
	v_mfma_f32_16x16x128_f8f6f4 v[72:75], v[24:31], v[204:211], v[72:75]
	v_mfma_f32_16x16x128_f8f6f4 v[52:55], v[16:23], v[212:219], v[52:55]
	v_mfma_f32_16x16x128_f8f6f4 v[48:51], v[24:31], v[212:219], v[48:51]
	v_mfma_f32_16x16x128_f8f6f4 v[60:63], v[16:23], v[220:227], v[60:63]
	v_mfma_f32_16x16x128_f8f6f4 v[56:59], v[24:31], v[220:227], v[56:59]
	v_mfma_f32_16x16x128_f8f6f4 v[36:39], v[16:23], v[228:235], v[36:39]
	v_mfma_f32_16x16x128_f8f6f4 v[32:35], v[24:31], v[228:235], v[32:35]
	s_setprio 0
	s_setprio 1
	v_mfma_f32_16x16x128_f8f6f4 v[100:103], v[0:7], v[204:211], v[100:103]
	v_mfma_f32_16x16x128_f8f6f4 v[96:99], v[8:15], v[204:211], v[96:99]
	v_mfma_f32_16x16x128_f8f6f4 v[84:87], v[0:7], v[212:219], v[84:87]
	v_mfma_f32_16x16x128_f8f6f4 v[80:83], v[8:15], v[212:219], v[80:83]
	v_mfma_f32_16x16x128_f8f6f4 v[68:71], v[0:7], v[220:227], v[68:71]
	v_mfma_f32_16x16x128_f8f6f4 v[64:67], v[8:15], v[220:227], v[64:67]
	v_mfma_f32_16x16x128_f8f6f4 v[44:47], v[0:7], v[228:235], v[44:47]
	v_mfma_f32_16x16x128_f8f6f4 v[40:43], v[8:15], v[228:235], v[40:43]
	s_setprio 0
	s_barrier
	ds_read_b128 v[4:7], v194
	ds_read_b128 v[8:11], v195
	ds_read_b128 v[0:3], v185
	ds_read_b128 v[16:19], v186
	ds_read_b128 v[12:15], v196
	ds_read_b128 v[20:23], v197
	ds_read_b128 v[24:27], v198
	ds_read_b128 v[28:31], v199
	s_add_u32 s28, s28, 0x20000
	s_addc_u32 s29, s29, 0
	s_mov_b32 m0, s34
	v_lshl_add_u64 v[236:237], s[28:29], 0, v[164:165]
	ds_read_b128 v[204:207], v200 offset:32768
	ds_read_b128 v[208:211], v200 offset:33792
	ds_read_b128 v[212:215], v200 offset:34816
	ds_read_b128 v[216:219], v200 offset:35840
	ds_read_b128 v[220:223], v200 offset:36864
	ds_read_b128 v[224:227], v200 offset:37888
	ds_read_b128 v[228:231], v200 offset:38912
	ds_read_b128 v[232:235], v200 offset:39936
	global_load_lds_dwordx4 v[236:237], off
	v_lshl_add_u64 v[236:237], s[28:29], 0, v[166:167]
	s_mov_b32 m0, s35
	s_nop 0
	global_load_lds_dwordx4 v[236:237], off
	s_waitcnt vmcnt(8)
	s_waitcnt lgkmcnt(0)
	s_barrier
	s_setprio 1
	s_waitcnt lgkmcnt(0)
	v_mfma_f32_16x16x128_f8f6f4 v[156:159], v[0:7], v[204:211], v[156:159]
	v_mfma_f32_16x16x128_f8f6f4 v[152:155], v[8:15], v[204:211], v[152:155]
	v_mfma_f32_16x16x128_f8f6f4 v[144:147], v[0:7], v[212:219], v[144:147]
	v_mfma_f32_16x16x128_f8f6f4 v[136:139], v[8:15], v[212:219], v[136:139]
	v_mfma_f32_16x16x128_f8f6f4 v[128:131], v[0:7], v[220:227], v[128:131]
	v_mfma_f32_16x16x128_f8f6f4 v[120:123], v[8:15], v[220:227], v[120:123]
	v_mfma_f32_16x16x128_f8f6f4 v[112:115], v[0:7], v[228:235], v[112:115]
	v_mfma_f32_16x16x128_f8f6f4 v[104:107], v[8:15], v[228:235], v[104:107]
	s_setprio 0
	s_setprio 1
	v_mfma_f32_16x16x128_f8f6f4 v[148:151], v[16:23], v[204:211], v[148:151]
	v_mfma_f32_16x16x128_f8f6f4 v[140:143], v[24:31], v[204:211], v[140:143]
	v_mfma_f32_16x16x128_f8f6f4 v[132:135], v[16:23], v[212:219], v[132:135]
	v_mfma_f32_16x16x128_f8f6f4 v[124:127], v[24:31], v[212:219], v[124:127]
	v_mfma_f32_16x16x128_f8f6f4 v[116:119], v[16:23], v[220:227], v[116:119]
	v_mfma_f32_16x16x128_f8f6f4 v[108:111], v[24:31], v[220:227], v[108:111]
	v_mfma_f32_16x16x128_f8f6f4 v[92:95], v[16:23], v[228:235], v[92:95]
	v_mfma_f32_16x16x128_f8f6f4 v[88:91], v[24:31], v[228:235], v[88:91]
	s_setprio 0
	s_barrier
	s_mov_b32 m0, s37
	v_lshl_add_u64 v[174:175], v[174:175], 0, s[2:3]
	s_add_u32 s26, s26, 0x20080
	ds_read_b128 v[204:207], v200 offset:49152
	ds_read_b128 v[208:211], v200 offset:50176
	ds_read_b128 v[212:215], v200 offset:51200
	ds_read_b128 v[216:219], v200 offset:52224
	ds_read_b128 v[220:223], v200 offset:53248
	ds_read_b128 v[224:227], v200 offset:54272
	ds_read_b128 v[228:231], v200 offset:55296
	ds_read_b128 v[232:235], v200 offset:56320
	global_load_lds_dwordx4 v[174:175], off
	v_lshl_add_u64 v[174:175], v[176:177], 0, s[2:3]
	s_mov_b32 m0, s38
	s_addc_u32 s27, s27, 0
	global_load_lds_dwordx4 v[174:175], off
	v_lshl_add_u64 v[174:175], s[26:27], 0, v[162:163]
	s_mov_b32 m0, s41
	s_nop 0
	global_load_lds_dwordx4 v[174:175], off
	v_lshl_add_u64 v[174:175], s[26:27], 0, v[160:161]
	s_mov_b32 m0, s42
	s_nop 0
	global_load_lds_dwordx4 v[174:175], off
	v_lshl_add_u64 v[174:175], v[178:179], 0, s[2:3]
	s_mov_b32 m0, s39
	s_nop 0
	global_load_lds_dwordx4 v[174:175], off
	v_lshl_add_u64 v[174:175], v[180:181], 0, s[2:3]
	s_mov_b32 m0, s40
	s_nop 0
	global_load_lds_dwordx4 v[174:175], off
	s_waitcnt vmcnt(8)
	s_waitcnt lgkmcnt(0)
	s_barrier
	s_setprio 1
	s_waitcnt lgkmcnt(0)
	v_mfma_f32_16x16x128_f8f6f4 v[76:79], v[0:7], v[204:211], v[76:79]
	v_mfma_f32_16x16x128_f8f6f4 v[72:75], v[8:15], v[204:211], v[72:75]
	v_mfma_f32_16x16x128_f8f6f4 v[52:55], v[0:7], v[212:219], v[52:55]
	v_mfma_f32_16x16x128_f8f6f4 v[48:51], v[8:15], v[212:219], v[48:51]
	v_mfma_f32_16x16x128_f8f6f4 v[60:63], v[0:7], v[220:227], v[60:63]
	v_mfma_f32_16x16x128_f8f6f4 v[56:59], v[8:15], v[220:227], v[56:59]
	v_mfma_f32_16x16x128_f8f6f4 v[36:39], v[0:7], v[228:235], v[36:39]
	v_mfma_f32_16x16x128_f8f6f4 v[32:35], v[8:15], v[228:235], v[32:35]
	s_setprio 0
	s_setprio 1
	v_mfma_f32_16x16x128_f8f6f4 v[100:103], v[16:23], v[204:211], v[100:103]
	v_mfma_f32_16x16x128_f8f6f4 v[96:99], v[24:31], v[204:211], v[96:99]
	v_mfma_f32_16x16x128_f8f6f4 v[84:87], v[16:23], v[212:219], v[84:87]
	v_mfma_f32_16x16x128_f8f6f4 v[80:83], v[24:31], v[212:219], v[80:83]
	v_mfma_f32_16x16x128_f8f6f4 v[68:71], v[16:23], v[220:227], v[68:71]
	v_mfma_f32_16x16x128_f8f6f4 v[64:67], v[24:31], v[220:227], v[64:67]
	v_mfma_f32_16x16x128_f8f6f4 v[44:47], v[16:23], v[228:235], v[44:47]
	v_mfma_f32_16x16x128_f8f6f4 v[40:43], v[24:31], v[228:235], v[40:43]
	s_setprio 0
	s_barrier
	s_add_i32 s50, s50, 2
	s_add_u32 s24, s24, 0x100
	s_addc_u32 s25, s25, 0
	s_add_u32 s48, s48, 0x100
	s_addc_u32 s49, s49, 0
	s_cmp_gt_u32 s50, 5
	s_cbranch_scc0 .LBB0_2052
	s_nop 15
	s_nop 7
	s_and_b64 vcc, exec, s[4:5]
	s_cbranch_vccz .LBB0_2055
	s_barrier

.LBB0_2931:
	s_ashr_i32 s15, s14, 31
	s_lshl_b64 s[18:19], s[14:15], 18
	v_readlane_b32 s20, v254, 44
	v_readlane_b32 s21, v254, 45
	s_add_u32 s18, s20, s18
	s_addc_u32 s19, s21, s19
	s_and_b64 s[20:21], s[16:17], exec
	s_cselect_b32 s15, s19, s23
	s_cselect_b32 s54, s18, s22
	s_ashr_i32 s13, s12, 31
	s_lshl_b64 s[20:21], s[12:13], 18
	s_add_u32 s20, s28, s20
	s_addc_u32 s21, s29, s21
	s_and_b64 s[26:27], s[16:17], exec
	s_cselect_b32 s13, s21, s25
	s_cselect_b32 s55, s20, s24
	s_add_u32 s22, s22, 0x20080
	s_addc_u32 s23, s23, 0
	s_add_u32 s56, s24, 0x100
	v_mov_b32_e32 v64, 0
	s_addc_u32 s57, s25, 0
	s_mov_b32 s58, -2
	v_mov_b32_e32 v65, v64
	v_mov_b32_e32 v66, v64
	v_mov_b32_e32 v67, v64
	v_mov_b32_e32 v116, v64
	v_mov_b32_e32 v117, v64
	v_mov_b32_e32 v118, v64
	v_mov_b32_e32 v119, v64
	v_mov_b32_e32 v84, v64
	v_mov_b32_e32 v85, v64
	v_mov_b32_e32 v86, v64
	v_mov_b32_e32 v87, v64
	v_mov_b32_e32 v128, v64
	v_mov_b32_e32 v129, v64
	v_mov_b32_e32 v130, v64
	v_mov_b32_e32 v131, v64
	v_mov_b32_e32 v32, v64
	v_mov_b32_e32 v33, v64
	v_mov_b32_e32 v34, v64
	v_mov_b32_e32 v35, v64
	v_mov_b32_e32 v48, v64
	v_mov_b32_e32 v49, v64
	v_mov_b32_e32 v50, v64
	v_mov_b32_e32 v51, v64
	v_mov_b32_e32 v36, v64
	v_mov_b32_e32 v37, v64
	v_mov_b32_e32 v38, v64
	v_mov_b32_e32 v39, v64
	v_mov_b32_e32 v52, v64
	v_mov_b32_e32 v53, v64
	v_mov_b32_e32 v54, v64
	v_mov_b32_e32 v55, v64
	v_mov_b32_e32 v40, v64
	v_mov_b32_e32 v41, v64
	v_mov_b32_e32 v42, v64
	v_mov_b32_e32 v43, v64
	v_mov_b32_e32 v56, v64
	v_mov_b32_e32 v57, v64
	v_mov_b32_e32 v58, v64
	v_mov_b32_e32 v59, v64
	v_mov_b32_e32 v44, v64
	v_mov_b32_e32 v45, v64
	v_mov_b32_e32 v46, v64
	v_mov_b32_e32 v47, v64
	v_mov_b32_e32 v72, v64
	v_mov_b32_e32 v73, v64
	v_mov_b32_e32 v74, v64
	v_mov_b32_e32 v75, v64
	v_mov_b32_e32 v96, v64
	v_mov_b32_e32 v97, v64
	v_mov_b32_e32 v98, v64
	v_mov_b32_e32 v99, v64
	v_mov_b32_e32 v136, v64
	v_mov_b32_e32 v137, v64
	v_mov_b32_e32 v138, v64
	v_mov_b32_e32 v139, v64
	v_mov_b32_e32 v108, v64
	v_mov_b32_e32 v109, v64
	v_mov_b32_e32 v110, v64
	v_mov_b32_e32 v111, v64
	v_mov_b32_e32 v140, v64
	v_mov_b32_e32 v141, v64
	v_mov_b32_e32 v142, v64
	v_mov_b32_e32 v143, v64
	v_mov_b32_e32 v112, v64
	v_mov_b32_e32 v113, v64
	v_mov_b32_e32 v114, v64
	v_mov_b32_e32 v115, v64
	v_mov_b32_e32 v144, v64
	v_mov_b32_e32 v145, v64
	v_mov_b32_e32 v146, v64
	v_mov_b32_e32 v147, v64
	v_mov_b32_e32 v124, v64
	v_mov_b32_e32 v125, v64
	v_mov_b32_e32 v126, v64
	v_mov_b32_e32 v127, v64
	v_mov_b32_e32 v156, v64
	v_mov_b32_e32 v157, v64
	v_mov_b32_e32 v158, v64
	v_mov_b32_e32 v159, v64
	v_mov_b32_e32 v148, v64
	v_mov_b32_e32 v149, v64
	v_mov_b32_e32 v150, v64
	v_mov_b32_e32 v151, v64
	v_mov_b32_e32 v120, v64
	v_mov_b32_e32 v121, v64
	v_mov_b32_e32 v122, v64
	v_mov_b32_e32 v123, v64
	v_mov_b32_e32 v152, v64
	v_mov_b32_e32 v153, v64
	v_mov_b32_e32 v154, v64
	v_mov_b32_e32 v155, v64
	v_mov_b32_e32 v132, v64
	v_mov_b32_e32 v133, v64
	v_mov_b32_e32 v134, v64
	v_mov_b32_e32 v135, v64
	v_mov_b32_e32 v88, v64
	v_mov_b32_e32 v89, v64
	v_mov_b32_e32 v90, v64
	v_mov_b32_e32 v91, v64
	v_mov_b32_e32 v60, v64
	v_mov_b32_e32 v61, v64
	v_mov_b32_e32 v62, v64
	v_mov_b32_e32 v63, v64
	v_mov_b32_e32 v92, v64
	v_mov_b32_e32 v93, v64
	v_mov_b32_e32 v94, v64
	v_mov_b32_e32 v95, v64
	v_mov_b32_e32 v68, v64
	v_mov_b32_e32 v69, v64
	v_mov_b32_e32 v70, v64
	v_mov_b32_e32 v71, v64
	v_mov_b32_e32 v100, v64
	v_mov_b32_e32 v101, v64
	v_mov_b32_e32 v102, v64
	v_mov_b32_e32 v103, v64
	v_mov_b32_e32 v76, v64
	v_mov_b32_e32 v77, v64
	v_mov_b32_e32 v78, v64
	v_mov_b32_e32 v79, v64
	v_mov_b32_e32 v104, v64
	v_mov_b32_e32 v105, v64
	v_mov_b32_e32 v106, v64
	v_mov_b32_e32 v107, v64
	v_mov_b32_e32 v80, v64
	v_mov_b32_e32 v81, v64
	v_mov_b32_e32 v82, v64
	v_mov_b32_e32 v83, v64
	s_mov_b32 s99, 1
.LBB0_2932:
	s_waitcnt lgkmcnt(0)
	ds_read_b128 v[20:23], v188
	ds_read_b128 v[24:27], v189
	ds_read_b128 v[16:19], v183
	ds_read_b128 v[0:3], v184
	ds_read_b128 v[28:31], v190
	ds_read_b128 v[4:7], v191
	ds_read_b128 v[8:11], v192
	ds_read_b128 v[12:15], v193
	s_add_u32 s24, s22, 0xfffe0080
	s_addc_u32 s25, s23, -1
	s_cmp_eq_u32 s58, 4
	s_cselect_b32 s27, s15, s25
	s_cselect_b32 s26, s54, s24
	s_cselect_b32 s25, s13, s57
	s_cselect_b32 s24, s55, s56
	v_lshl_add_u64 v[232:233], s[22:23], 0, v[168:169]
	s_add_i32 m0, s33, 0xc000
	ds_read_b128 v[174:177], v200
	ds_read_b128 v[178:181], v200 offset:1024
	ds_read_b128 v[208:211], v200 offset:2048
	ds_read_b128 v[212:215], v200 offset:3072
	ds_read_b128 v[216:219], v200 offset:4096
	ds_read_b128 v[220:223], v200 offset:5120
	ds_read_b128 v[224:227], v200 offset:6144
	ds_read_b128 v[228:231], v200 offset:7168
	global_load_lds_dwordx4 v[232:233], off
	v_lshl_add_u64 v[232:233], s[22:23], 0, v[170:171]
	s_add_i32 m0, s33, 0xe000
	s_nop 0
	global_load_lds_dwordx4 v[232:233], off
	s_waitcnt vmcnt(24)
	s_cmp_lg_u32 s99, 0
	s_cbranch_scc1 .Lfk3_a
	s_waitcnt vmcnt(8)
.Lfk3_a:
	s_waitcnt lgkmcnt(0)
	s_barrier
	s_setprio 1
	s_waitcnt lgkmcnt(0)
	v_mfma_f32_16x16x128_f8f6f4 v[156:159], v[16:23], v[174:181], v[156:159]
	v_mfma_f32_16x16x128_f8f6f4 v[124:127], v[24:31], v[174:181], v[124:127]
	v_mfma_f32_16x16x128_f8f6f4 v[144:147], v[16:23], v[208:215], v[144:147]
	v_mfma_f32_16x16x128_f8f6f4 v[112:115], v[24:31], v[208:215], v[112:115]
	v_mfma_f32_16x16x128_f8f6f4 v[140:143], v[16:23], v[216:223], v[140:143]
	v_mfma_f32_16x16x128_f8f6f4 v[108:111], v[24:31], v[216:223], v[108:111]
	v_mfma_f32_16x16x128_f8f6f4 v[136:139], v[16:23], v[224:231], v[136:139]
	v_mfma_f32_16x16x128_f8f6f4 v[96:99], v[24:31], v[224:231], v[96:99]
	s_setprio 0
	s_setprio 1
	v_mfma_f32_16x16x128_f8f6f4 v[72:75], v[0:7], v[174:181], v[72:75]
	v_mfma_f32_16x16x128_f8f6f4 v[44:47], v[8:15], v[174:181], v[44:47]
	v_mfma_f32_16x16x128_f8f6f4 v[56:59], v[0:7], v[208:215], v[56:59]
	v_mfma_f32_16x16x128_f8f6f4 v[40:43], v[8:15], v[208:215], v[40:43]
	v_mfma_f32_16x16x128_f8f6f4 v[52:55], v[0:7], v[216:223], v[52:55]
	v_mfma_f32_16x16x128_f8f6f4 v[36:39], v[8:15], v[216:223], v[36:39]
	v_mfma_f32_16x16x128_f8f6f4 v[48:51], v[0:7], v[224:231], v[48:51]
	v_mfma_f32_16x16x128_f8f6f4 v[32:35], v[8:15], v[224:231], v[32:35]
	s_setprio 0
	s_barrier
	s_mov_b32 m0, s34
	v_lshl_add_u64 v[174:175], s[24:25], 0, v[162:163]
	s_add_u32 s60, s24, 0x20000
	ds_read_b128 v[208:211], v200 offset:16384
	ds_read_b128 v[212:215], v200 offset:17408
	ds_read_b128 v[216:219], v200 offset:18432
	ds_read_b128 v[220:223], v200 offset:19456
	ds_read_b128 v[224:227], v200 offset:20480
	ds_read_b128 v[228:231], v200 offset:21504
	ds_read_b128 v[232:235], v200 offset:22528
	ds_read_b128 v[236:239], v200 offset:23552
	global_load_lds_dwordx4 v[174:175], off
	v_lshl_add_u64 v[176:177], s[24:25], 0, v[160:161]
	s_mov_b32 m0, s35
	s_addc_u32 s61, s25, 0
	global_load_lds_dwordx4 v[176:177], off
	v_lshl_add_u64 v[178:179], s[60:61], 0, v[162:163]
	s_mov_b32 m0, s36
	v_lshl_add_u64 v[180:181], s[26:27], 0, v[166:167]
	global_load_lds_dwordx4 v[178:179], off
	v_lshl_add_u64 v[178:179], s[60:61], 0, v[160:161]
	s_mov_b32 m0, s37
	s_nop 0
	global_load_lds_dwordx4 v[178:179], off
	v_lshl_add_u64 v[178:179], s[26:27], 0, v[164:165]
	s_mov_b32 m0, s33
	s_nop 0
	global_load_lds_dwordx4 v[178:179], off
	s_mov_b32 m0, s38
	s_nop 0
	global_load_lds_dwordx4 v[180:181], off
	s_waitcnt vmcnt(24)
	s_cmp_lg_u32 s99, 0
	s_cbranch_scc1 .Lfk3_b
	s_waitcnt vmcnt(8)
.Lfk3_b:
	s_mov_b32 s99, 0
	s_waitcnt lgkmcnt(0)
	s_barrier
	s_setprio 1
	s_waitcnt lgkmcnt(0)
	v_mfma_f32_16x16x128_f8f6f4 v[128:131], v[16:23], v[208:215], v[128:131]
	v_mfma_f32_16x16x128_f8f6f4 v[84:87], v[24:31], v[208:215], v[84:87]
	v_mfma_f32_16x16x128_f8f6f4 v[116:119], v[16:23], v[216:223], v[116:119]
	v_mfma_f32_16x16x128_f8f6f4 v[64:67], v[24:31], v[216:223], v[64:67]
	v_mfma_f32_16x16x128_f8f6f4 v[148:151], v[16:23], v[224:231], v[148:151]
	v_mfma_f32_16x16x128_f8f6f4 v[120:123], v[24:31], v[224:231], v[120:123]
	v_mfma_f32_16x16x128_f8f6f4 v[152:155], v[16:23], v[232:239], v[152:155]
	v_mfma_f32_16x16x128_f8f6f4 v[132:135], v[24:31], v[232:239], v[132:135]
	s_setprio 0
	s_setprio 1
	v_mfma_f32_16x16x128_f8f6f4 v[88:91], v[0:7], v[208:215], v[88:91]
	v_mfma_f32_16x16x128_f8f6f4 v[60:63], v[8:15], v[208:215], v[60:63]
	v_mfma_f32_16x16x128_f8f6f4 v[92:95], v[0:7], v[216:223], v[92:95]
	v_mfma_f32_16x16x128_f8f6f4 v[68:71], v[8:15], v[216:223], v[68:71]
	v_mfma_f32_16x16x128_f8f6f4 v[100:103], v[0:7], v[224:231], v[100:103]
	v_mfma_f32_16x16x128_f8f6f4 v[76:79], v[8:15], v[224:231], v[76:79]
	v_mfma_f32_16x16x128_f8f6f4 v[104:107], v[0:7], v[232:239], v[104:107]
	v_mfma_f32_16x16x128_f8f6f4 v[80:83], v[8:15], v[232:239], v[80:83]
	s_setprio 0
	s_barrier
	ds_read_b128 v[4:7], v194
	ds_read_b128 v[8:11], v195
	ds_read_b128 v[0:3], v185
	ds_read_b128 v[16:19], v186
	ds_read_b128 v[12:15], v196
	ds_read_b128 v[20:23], v197
	ds_read_b128 v[24:27], v198
	ds_read_b128 v[28:31], v199
	s_add_u32 s26, s26, 0x20000
	s_addc_u32 s27, s27, 0
	s_mov_b32 m0, s39
	v_lshl_add_u64 v[240:241], s[26:27], 0, v[164:165]
	ds_read_b128 v[208:211], v200 offset:32768
	ds_read_b128 v[212:215], v200 offset:33792
	ds_read_b128 v[216:219], v200 offset:34816
	ds_read_b128 v[220:223], v200 offset:35840
	ds_read_b128 v[224:227], v200 offset:36864
	ds_read_b128 v[228:231], v200 offset:37888
	ds_read_b128 v[232:235], v200 offset:38912
	ds_read_b128 v[236:239], v200 offset:39936
	global_load_lds_dwordx4 v[240:241], off
	v_lshl_add_u64 v[240:241], s[26:27], 0, v[166:167]
	s_mov_b32 m0, s40
	s_nop 0
	global_load_lds_dwordx4 v[240:241], off
	s_waitcnt vmcnt(8)
	s_waitcnt lgkmcnt(0)
	s_barrier
	s_setprio 1
	s_waitcnt lgkmcnt(0)
	v_mfma_f32_16x16x128_f8f6f4 v[156:159], v[0:7], v[208:215], v[156:159]
	v_mfma_f32_16x16x128_f8f6f4 v[124:127], v[8:15], v[208:215], v[124:127]
	v_mfma_f32_16x16x128_f8f6f4 v[144:147], v[0:7], v[216:223], v[144:147]
	v_mfma_f32_16x16x128_f8f6f4 v[112:115], v[8:15], v[216:223], v[112:115]
	v_mfma_f32_16x16x128_f8f6f4 v[140:143], v[0:7], v[224:231], v[140:143]
	v_mfma_f32_16x16x128_f8f6f4 v[108:111], v[8:15], v[224:231], v[108:111]
	v_mfma_f32_16x16x128_f8f6f4 v[136:139], v[0:7], v[232:239], v[136:139]
	v_mfma_f32_16x16x128_f8f6f4 v[96:99], v[8:15], v[232:239], v[96:99]
	s_setprio 0
	s_setprio 1
	v_mfma_f32_16x16x128_f8f6f4 v[72:75], v[16:23], v[208:215], v[72:75]
	v_mfma_f32_16x16x128_f8f6f4 v[44:47], v[24:31], v[208:215], v[44:47]
	v_mfma_f32_16x16x128_f8f6f4 v[56:59], v[16:23], v[216:223], v[56:59]
	v_mfma_f32_16x16x128_f8f6f4 v[40:43], v[24:31], v[216:223], v[40:43]
	v_mfma_f32_16x16x128_f8f6f4 v[52:55], v[16:23], v[224:231], v[52:55]
	v_mfma_f32_16x16x128_f8f6f4 v[36:39], v[24:31], v[224:231], v[36:39]
	v_mfma_f32_16x16x128_f8f6f4 v[48:51], v[16:23], v[232:239], v[48:51]
	v_mfma_f32_16x16x128_f8f6f4 v[32:35], v[24:31], v[232:239], v[32:35]
	s_setprio 0
	s_barrier
	s_mov_b32 m0, s42
	v_lshl_add_u64 v[174:175], v[174:175], 0, s[8:9]
	s_add_u32 s24, s24, 0x20080
	ds_read_b128 v[208:211], v200 offset:49152
	ds_read_b128 v[212:215], v200 offset:50176
	ds_read_b128 v[216:219], v200 offset:51200
	ds_read_b128 v[220:223], v200 offset:52224
	ds_read_b128 v[224:227], v200 offset:53248
	ds_read_b128 v[228:231], v200 offset:54272
	ds_read_b128 v[232:235], v200 offset:55296
	ds_read_b128 v[236:239], v200 offset:56320
	global_load_lds_dwordx4 v[174:175], off
	v_lshl_add_u64 v[174:175], v[176:177], 0, s[8:9]
	s_mov_b32 m0, s43
	s_addc_u32 s25, s25, 0
	global_load_lds_dwordx4 v[174:175], off
	v_lshl_add_u64 v[174:175], s[24:25], 0, v[162:163]
	s_mov_b32 m0, s46
	s_nop 0
	global_load_lds_dwordx4 v[174:175], off
	v_lshl_add_u64 v[174:175], s[24:25], 0, v[160:161]
	s_mov_b32 m0, s47
	s_nop 0
	global_load_lds_dwordx4 v[174:175], off
	v_lshl_add_u64 v[174:175], v[178:179], 0, s[8:9]
	s_mov_b32 m0, s44
	s_nop 0
	global_load_lds_dwordx4 v[174:175], off
	v_lshl_add_u64 v[174:175], v[180:181], 0, s[8:9]
	s_mov_b32 m0, s45
	s_nop 0
	global_load_lds_dwordx4 v[174:175], off
	s_waitcnt vmcnt(8)
	s_waitcnt lgkmcnt(0)
	s_barrier
	s_setprio 1
	s_waitcnt lgkmcnt(0)
	v_mfma_f32_16x16x128_f8f6f4 v[128:131], v[0:7], v[208:215], v[128:131]
	v_mfma_f32_16x16x128_f8f6f4 v[84:87], v[8:15], v[208:215], v[84:87]
	v_mfma_f32_16x16x128_f8f6f4 v[116:119], v[0:7], v[216:223], v[116:119]
	v_mfma_f32_16x16x128_f8f6f4 v[64:67], v[8:15], v[216:223], v[64:67]
	v_mfma_f32_16x16x128_f8f6f4 v[148:151], v[0:7], v[224:231], v[148:151]
	v_mfma_f32_16x16x128_f8f6f4 v[120:123], v[8:15], v[224:231], v[120:123]
	v_mfma_f32_16x16x128_f8f6f4 v[152:155], v[0:7], v[232:239], v[152:155]
	v_mfma_f32_16x16x128_f8f6f4 v[132:135], v[8:15], v[232:239], v[132:135]
	s_setprio 0
	s_setprio 1
	v_mfma_f32_16x16x128_f8f6f4 v[88:91], v[16:23], v[208:215], v[88:91]
	v_mfma_f32_16x16x128_f8f6f4 v[60:63], v[24:31], v[208:215], v[60:63]
	v_mfma_f32_16x16x128_f8f6f4 v[92:95], v[16:23], v[216:223], v[92:95]
	v_mfma_f32_16x16x128_f8f6f4 v[68:71], v[24:31], v[216:223], v[68:71]
	v_mfma_f32_16x16x128_f8f6f4 v[100:103], v[16:23], v[224:231], v[100:103]
	v_mfma_f32_16x16x128_f8f6f4 v[76:79], v[24:31], v[224:231], v[76:79]
	v_mfma_f32_16x16x128_f8f6f4 v[104:107], v[16:23], v[232:239], v[104:107]
	v_mfma_f32_16x16x128_f8f6f4 v[80:83], v[24:31], v[232:239], v[80:83]
	s_setprio 0
	s_barrier
	s_add_i32 s58, s58, 2
	s_add_u32 s22, s22, 0x100
	s_addc_u32 s23, s23, 0
	s_add_u32 s56, s56, 0x100
	s_addc_u32 s57, s57, 0
	s_cmp_gt_u32 s58, 5
	s_cbranch_scc0 .LBB0_2932
	s_nop 15
	s_nop 7
	s_and_b64 vcc, exec, s[10:11]
	s_cbranch_vccz .LBB0_2935
	s_barrier
